# T3a stage E: causal mask of the 16 accumulator values = one compare with inline constant + one select each (3 rotating mask registers) instead of ~11 instr + nops per value
# baseline (speedup 1.0000x reference)
; __device__ __forceinline__ int crow(int reg, int h) { return (reg & 3) + 8 * (reg >> 2) + 4 * h; }
; __device__ __forceinline__ f32x16 zero16() { return (f32x16){0.f, 0.f, 0.f, 0.f, 0.f, 0.f, 0.f, 0.f, 0.f, 0.f, 0.f, 0.f, 0.f, 0.f, 0.f, 0.f}; }
; __device__ __forceinline__ void phase1(const int WID_, const In& I, char* lds) {
;     ...
;         for (int task = wv; task < 12; task += 8) {
;             const int mat = task / 3, tt = task % 3, st = (tt == 0) ? 0 : 1, jt = (tt == 2) ? 1 : 0;
;             const bf16* Asrc = MAT((mat & 1) ? O_KB : O_BB) + 32 * jt * LD;
;             const bf16* Bsrc = MAT((mat >> 1) ? O_RB : O_AB) + 32 * st * LD;
;             f32x16 acc = mm_tile<64>(zero16(), Asrc, LD, Bsrc, LD, lane);
;             const int cs = 32 * st + (lane & 31), hh = lane >> 5; const bool incl = (mat >> 1) != 0;
; #pragma unroll
;             for (int rg = 0; rg < 16; ++rg) { const int j = 32 * jt + crow(rg, hh); const bool keep = incl ? (j <= cs) : (j < cs); if (!keep) acc[rg] = 0.f; }
;             store_tr(acc, MAT(O_NM + mat * MB) + 32 * st * LD + 32 * jt, LD, lane);
.LBB0_1431:
	s_mul_hi_u32 s0, s4, 0xaaaaaaab
	s_lshr_b32 s42, s0, 1
	s_mul_i32 s1, s42, -3
	s_add_i32 s41, s4, s1
	s_bfe_u32 s0, s0, 0x10001
	s_cmp_eq_u32 s0, 0
	s_movk_i32 s0, 0x4800
	s_cselect_b32 s0, s0, 0x6c00
	s_add_i32 s0, s0, 0
	s_cmp_eq_u32 s41, 2
	s_cselect_b32 s43, 32, 0
	s_mul_i32 s1, s43, 0x90
	s_add_i32 s44, s0, s1
	s_cmp_lt_u32 s4, 6
	s_cselect_b64 vcc, -1, 0
	s_and_b64 s[0:1], vcc, exec
	s_cselect_b32 s0, 0, 0x2400
	s_add_i32 s45, s0, 0
	s_cmp_eq_u32 s41, 0
	v_add3_u32 v63, s44, v60, v61
	s_cselect_b64 s[6:7], -1, 0
	ds_read_b128 v[0:3], v63
	s_and_b64 s[0:1], s[6:7], exec
	s_cselect_b32 s0, 0, 32
	s_mul_i32 s44, s0, 0x90
	s_add_i32 s45, s45, s44
	v_add3_u32 v68, s45, v60, v61
	ds_read_b128 v[4:7], v68
	ds_read_b128 v[64:67], v63 offset:32
	ds_read_b128 v[70:73], v68 offset:32
	s_waitcnt lgkmcnt(2)
	v_mfma_f32_32x32x16_bf16 v[0:15], v[0:3], v[4:7], 0
	ds_read_b128 v[80:83], v63 offset:64
	ds_read_b128 v[84:87], v63 offset:96
	v_add_u32_e32 v74, s43, v52
	v_or_b32_e32 v63, s0, v78
	v_cndmask_b32_e64 v88, 0, 1, vcc
	s_mulk_i32 s42, 0x2400
	v_sub_u32_e32 v75, v63, v74
	s_waitcnt lgkmcnt(2)
	v_mfma_f32_32x32x16_bf16 v[0:15], v[64:67], v[70:73], v[0:15]
	ds_read_b128 v[64:67], v68 offset:64
	ds_read_b128 v[70:73], v68 offset:96
	v_sub_u32_e32 v75, v75, v88
	v_add_u32_e32 v75, 1, v75
	s_waitcnt lgkmcnt(1)
	v_mfma_f32_32x32x16_bf16 v[0:15], v[80:83], v[64:67], v[0:15]
	s_waitcnt lgkmcnt(0)
	v_mfma_f32_32x32x16_bf16 v[0:15], v[84:87], v[70:73], v[0:15]
	s_add_i32 s0, s42, 0
	s_add_i32 s0, s0, s44
	s_lshl_b32 s1, s43, 1
	s_add_i32 s0, s0, s1
	s_add_i32 s0, s0, 0x14400
	v_add3_u32 v63, s0, v60, v62
	v_cmp_lt_i32_e32 vcc, 0, v75
	v_cmp_lt_i32_e64 s[98:99], 1, v75
	v_cmp_lt_i32_e64 s[100:101], 2, v75
	s_nop 2
	v_cndmask_b32_e32 v0, 0, v0, vcc
	v_cmp_lt_i32_e32 vcc, 3, v75
	v_cndmask_b32_e64 v1, 0, v1, s[98:99]
	v_cmp_lt_i32_e64 s[98:99], 8, v75
	v_cndmask_b32_e64 v2, 0, v2, s[100:101]
	v_cmp_lt_i32_e64 s[100:101], 9, v75
	v_cndmask_b32_e32 v3, 0, v3, vcc
	v_cmp_lt_i32_e32 vcc, 10, v75
	v_cndmask_b32_e64 v4, 0, v4, s[98:99]
	v_cmp_lt_i32_e64 s[98:99], 11, v75
	v_cndmask_b32_e64 v5, 0, v5, s[100:101]
	v_cmp_lt_i32_e64 s[100:101], 16, v75
	v_cndmask_b32_e32 v6, 0, v6, vcc
	v_cmp_lt_i32_e32 vcc, 17, v75
	v_cndmask_b32_e64 v7, 0, v7, s[98:99]
	v_cmp_lt_i32_e64 s[98:99], 18, v75
	v_cndmask_b32_e64 v8, 0, v8, s[100:101]
	v_cmp_lt_i32_e64 s[100:101], 19, v75
	v_cndmask_b32_e32 v9, 0, v9, vcc
	v_cmp_lt_i32_e32 vcc, 24, v75
	v_cndmask_b32_e64 v10, 0, v10, s[98:99]
	v_cmp_lt_i32_e64 s[98:99], 25, v75
	v_cndmask_b32_e64 v11, 0, v11, s[100:101]
	v_cmp_lt_i32_e64 s[100:101], 26, v75
	v_cndmask_b32_e32 v12, 0, v12, vcc
	v_cmp_lt_i32_e32 vcc, 27, v75
	v_cndmask_b32_e64 v13, 0, v13, s[98:99]
	v_cndmask_b32_e64 v14, 0, v14, s[100:101]
	v_cndmask_b32_e32 v15, 0, v15, vcc
	v_cvt_pk_bf16_f32 v64, v0, v1
	v_cvt_pk_bf16_f32 v65, v2, v3
	v_cvt_pk_bf16_f32 v66, v4, v5
	v_cvt_pk_bf16_f32 v67, v6, v7
	ds_write2_b64 v63, v[64:65], v[66:67] offset1:2
	v_cvt_pk_bf16_f32 v64, v8, v9
	v_cvt_pk_bf16_f32 v65, v10, v11
	v_cvt_pk_bf16_f32 v66, v12, v13
	v_cvt_pk_bf16_f32 v67, v14, v15
	s_cmp_gt_u32 s4, 2
	ds_write2_b64 v63, v[64:65], v[66:67] offset0:4 offset1:6
	s_cbranch_scc1 .LBB0_1430
	s_cmp_lt_i32 s41, 2
	s_cbranch_scc1 .LBB0_1434
	s_cmp_eq_u32 s41, 2
	s_cselect_b64 s[0:1], -1, 0
	s_cbranch_execz .LBB0_1435
	s_branch .LBB0_1436
